# U sweep: LDS wait only on the token-change path (record read latency overlaps the dots)
# speedup vs baseline: 1.0027x; 1.0019x over previous
; #define LAS __attribute__((address_space(3)))
; #define PE_VMW "vmcnt(" PE_STR(PE_VMY) ")"
; #define PE_ISSUE_U(S, rec_) PE_ISSUE4(S, rec_, UB8)
; #define PE_WAIT4U(S, cntstr) asm volatile("s_waitcnt " cntstr : "+v"(ru4[S][0]), "+v"(ru4[S][1]), "+v"(ru4[S][2]), "+v"(ru4[S][3]) :: "memory")
;     ...
;     {
;         unsigned er[PE_RD];
; #pragma unroll
;         for (int q = 0; q < PE_RD; ++q) { const v4u rec = *(const LAS v4u*)(ents + 4 * q); er[q] = __builtin_amdgcn_readfirstlane(rec.x); PE_ISSUE_U(q, rec); }
;         int jcur = (int)((er[0] >> 14) & 3u);
;         v4u hcur = *(const LAS v4u*)(hql + (jcur * 64 + lane) * 4);
;         v4u nrec = *(const LAS v4u*)(ents + 4 * PE_RD);
; #pragma unroll 1
;         for (int bi = 0; bi < nb; bi += PE_RD) {
; #pragma unroll
;             for (int q = 0; q < PE_RD; ++q) {
;                 PE_WAIT4U(q, PE_VMW);
;                 PE_UBATCH(q, er[q]);
;                 er[q] = __builtin_amdgcn_readfirstlane(nrec.x);
;                 PE_ISSUE_U(q, nrec);
;                 nrec = *(const LAS v4u*)(ents + 4 * (bi + q + PE_RD + 1));
;             }
.LBB0_2832:
	s_or_b64 exec, exec, s[0:1]
	v_cmp_gt_i32_e32 vcc, 6, v50
	s_and_saveexec_b64 s[0:1], vcc
	v_add_u32_e32 v0, s6, v50
	v_lshl_add_u32 v0, v0, 4, s90
	ds_write_b128 v0, v[122:125] offset:6720
	s_or_b64 exec, exec, s[0:1]
	s_waitcnt lgkmcnt(0)
	v_mov_b32_e32 v5, s90
	ds_read_b128 v[0:3], v5 offset:6720
	v_lshlrev_b32_e32 v118, 3, v50
	v_and_b32_e32 v43, 31, v50
	v_cmp_lt_u32_e64 s[100:101], 31, v50
	v_lshlrev_b32_e32 v43, 4, v43
	v_lshl_add_u32 v52, v43, 1, s90
	s_cmp_gt_i32 s6, 0
	s_cselect_b64 s[2:3], -1, 0
	s_cmp_lt_i32 s6, 1
	s_waitcnt lgkmcnt(0)
	v_readfirstlane_b32 s10, v0
	v_and_b32_e32 v48, 0x3fff, v0
	v_cndmask_b32_e64 v48, v48, v1, s[100:101]
	v_lshl_add_u32 v48, v48, 9, v43
	global_load_dwordx4 v[8:11], v48, s[70:71]
	v_cndmask_b32_e64 v48, v2, v3, s[100:101]
	v_lshl_add_u32 v48, v48, 9, v43
	global_load_dwordx4 v[12:15], v48, s[70:71]
	ds_read_b128 v[0:3], v5 offset:6736
	s_waitcnt lgkmcnt(0)
	v_readfirstlane_b32 s11, v0
	v_and_b32_e32 v48, 0x3fff, v0
	v_cndmask_b32_e64 v48, v48, v1, s[100:101]
	v_lshl_add_u32 v48, v48, 9, v43
	global_load_dwordx4 v[16:19], v48, s[70:71]
	v_cndmask_b32_e64 v48, v2, v3, s[100:101]
	v_lshl_add_u32 v48, v48, 9, v43
	global_load_dwordx4 v[20:23], v48, s[70:71]
	ds_read_b128 v[0:3], v5 offset:6752
	s_waitcnt lgkmcnt(0)
	v_readfirstlane_b32 s12, v0
	v_and_b32_e32 v48, 0x3fff, v0
	v_cndmask_b32_e64 v48, v48, v1, s[100:101]
	v_lshl_add_u32 v48, v48, 9, v43
	global_load_dwordx4 v[24:27], v48, s[70:71]
	v_cndmask_b32_e64 v48, v2, v3, s[100:101]
	v_lshl_add_u32 v48, v48, 9, v43
	global_load_dwordx4 v[28:31], v48, s[70:71]
	s_cbranch_scc1 .LBB0_2861
	s_bfe_u32 s9, s10, 0x2000e
	v_lshl_add_u32 v48, s9, 10, v52
	ds_read_b128 v[0:3], v48 offset:11072
	ds_read_b128 v[44:47], v48 offset:11088
	v_and_b32_e32 v4, 15, v50
	v_bfe_u32 v33, v50, 4, 1
	v_cmp_eq_u32_e32 vcc, 0, v4
	v_lshrrev_b32_e32 v4, 5, v50
	s_mov_b32 s7, 0
	v_lshl_add_u32 v33, v33, 1, v4
	v_readlane_b32 s8, v255, 2
	s_nop 1
	v_mov_b32_e32 v136, s8
	s_waitcnt lgkmcnt(0)
.LBB0_2838:
	ds_read_b128 v[4:7], v136
	s_waitcnt vmcnt(4)
	s_bfe_u32 s0, s10, 0x30010
	s_cmp_lg_u32 s0, 0
	s_cbranch_scc0 .Lu16_skip0
	s_bfe_u32 s1, s10, 0x2000e
	s_cmp_eq_u32 s1, s9
	s_cbranch_scc1 .Lu16_same0
	v_lshl_add_u32 v48, s1, 10, v52
	ds_read_b128 v[0:3], v48 offset:11072
	ds_read_b128 v[44:47], v48 offset:11088
	s_mov_b32 s9, s1
	s_waitcnt lgkmcnt(0)
.Lu16_same0:
	v_dot8_i32_i4 v39, v8, v0, 0
	v_dot8_i32_i4 v40, v12, v0, 0
	v_dot8_i32_i4 v35, v8, v2, 0
	v_dot8_i32_i4 v36, v12, v2, 0
	v_dot8_i32_i4 v39, v9, v1, v39
	v_dot8_i32_i4 v40, v13, v1, v40
	v_dot8_i32_i4 v35, v9, v3, v35
	v_dot8_i32_i4 v36, v13, v3, v36
	v_dot8_i32_i4 v39, v10, v44, v39
	v_dot8_i32_i4 v40, v14, v44, v40
	v_dot8_i32_i4 v35, v10, v46, v35
	v_dot8_i32_i4 v36, v14, v46, v36
	v_dot8_i32_i4 v39, v11, v45, v39
	v_dot8_i32_i4 v40, v15, v45, v40
	v_dot8_i32_i4 v35, v11, v47, v35
	v_dot8_i32_i4 v36, v15, v47, v36
	s_nop 2
	v_lshl_add_u32 v39, v39, 4, v35
	v_lshl_add_u32 v40, v40, 4, v36
	s_mulk_i32 s1, 0x690
	s_nop 0
	v_permlane16_swap_b32_e32 v39, v40
	v_add_u32_e32 v39, v39, v40
	s_lshr_b32 s4, s10, 17
	s_add_i32 s1, s90, s1
	v_add_u32_dpp v39, v39, v39 quad_perm:[1,0,3,2] row_mask:0xf bank_mask:0xf bound_ctrl:1
	s_and_b32 s4, s4, 0x7ffc
	s_add_i32 s1, s1, s4
	v_add_u32_dpp v39, v39, v39 quad_perm:[2,3,0,1] row_mask:0xf bank_mask:0xf bound_ctrl:1
	v_lshl_add_u32 v34, v33, 2, s1
	s_nop 0
	v_add_u32_dpp v41, v39, v39 row_half_mirror row_mask:0xf bank_mask:0xf bound_ctrl:1
	s_nop 1
	v_mov_b32_dpp v42, v41 row_mirror row_mask:0xf bank_mask:0xf bound_ctrl:1
	v_add_u32_e32 v42, v41, v42
	s_and_saveexec_b64 s[0:1], vcc
	ds_write_b32 v34, v42
	s_or_b64 exec, exec, s[0:1]
; #define LAS __attribute__((address_space(3)))
; #define PE_VMW "vmcnt(" PE_STR(PE_VMY) ")"
; #define PE_ISSUE_U(S, rec_) PE_ISSUE4(S, rec_, UB8)
; #define PE_WAIT4U(S, cntstr) asm volatile("s_waitcnt " cntstr : "+v"(ru4[S][0]), "+v"(ru4[S][1]), "+v"(ru4[S][2]), "+v"(ru4[S][3]) :: "memory")
;     ...
;     {
;         unsigned er[PE_RD];
; #pragma unroll
;         for (int q = 0; q < PE_RD; ++q) { const v4u rec = *(const LAS v4u*)(ents + 4 * q); er[q] = __builtin_amdgcn_readfirstlane(rec.x); PE_ISSUE_U(q, rec); }
;         int jcur = (int)((er[0] >> 14) & 3u);
;         v4u hcur = *(const LAS v4u*)(hql + (jcur * 64 + lane) * 4);
;         v4u nrec = *(const LAS v4u*)(ents + 4 * PE_RD);
; #pragma unroll 1
;         for (int bi = 0; bi < nb; bi += PE_RD) {
; #pragma unroll
;             for (int q = 0; q < PE_RD; ++q) {
;                 PE_WAIT4U(q, PE_VMW);
;                 PE_UBATCH(q, er[q]);
;                 er[q] = __builtin_amdgcn_readfirstlane(nrec.x);
;                 PE_ISSUE_U(q, nrec);
;                 nrec = *(const LAS v4u*)(ents + 4 * (bi + q + PE_RD + 1));
;             }
.Lu16_skip0:
	s_waitcnt lgkmcnt(0)
	v_readfirstlane_b32 s10, v4
	v_and_b32_e32 v48, 0x3fff, v4
	v_cndmask_b32_e64 v48, v48, v5, s[100:101]
	v_lshl_add_u32 v48, v48, 9, v43
	global_load_dwordx4 v[8:11], v48, s[70:71]
	v_cndmask_b32_e64 v48, v6, v7, s[100:101]
	v_lshl_add_u32 v48, v48, 9, v43
	global_load_dwordx4 v[12:15], v48, s[70:71]
	ds_read_b128 v[4:7], v136 offset:16
	s_waitcnt vmcnt(4)
	s_bfe_u32 s0, s11, 0x30010
	s_cmp_lg_u32 s0, 0
	s_cbranch_scc0 .Lu16_skip1
	s_bfe_u32 s1, s11, 0x2000e
	s_cmp_eq_u32 s1, s9
	s_cbranch_scc1 .Lu16_same1
	v_lshl_add_u32 v48, s1, 10, v52
	ds_read_b128 v[0:3], v48 offset:11072
	ds_read_b128 v[44:47], v48 offset:11088
	s_mov_b32 s9, s1
	s_waitcnt lgkmcnt(0)
.Lu16_same1:
	v_dot8_i32_i4 v39, v16, v0, 0
	v_dot8_i32_i4 v40, v20, v0, 0
	v_dot8_i32_i4 v35, v16, v2, 0
	v_dot8_i32_i4 v36, v20, v2, 0
	v_dot8_i32_i4 v39, v17, v1, v39
	v_dot8_i32_i4 v40, v21, v1, v40
	v_dot8_i32_i4 v35, v17, v3, v35
	v_dot8_i32_i4 v36, v21, v3, v36
	v_dot8_i32_i4 v39, v18, v44, v39
	v_dot8_i32_i4 v40, v22, v44, v40
	v_dot8_i32_i4 v35, v18, v46, v35
	v_dot8_i32_i4 v36, v22, v46, v36
	v_dot8_i32_i4 v39, v19, v45, v39
	v_dot8_i32_i4 v40, v23, v45, v40
	v_dot8_i32_i4 v35, v19, v47, v35
	v_dot8_i32_i4 v36, v23, v47, v36
	s_nop 2
	v_lshl_add_u32 v39, v39, 4, v35
	v_lshl_add_u32 v40, v40, 4, v36
	s_mulk_i32 s1, 0x690
	s_nop 0
	v_permlane16_swap_b32_e32 v39, v40
	v_add_u32_e32 v39, v39, v40
	s_lshr_b32 s4, s11, 17
	s_add_i32 s1, s90, s1
	v_add_u32_dpp v39, v39, v39 quad_perm:[1,0,3,2] row_mask:0xf bank_mask:0xf bound_ctrl:1
	s_and_b32 s4, s4, 0x7ffc
	s_add_i32 s1, s1, s4
	v_add_u32_dpp v39, v39, v39 quad_perm:[2,3,0,1] row_mask:0xf bank_mask:0xf bound_ctrl:1
	v_lshl_add_u32 v34, v33, 2, s1
	s_nop 0
	v_add_u32_dpp v41, v39, v39 row_half_mirror row_mask:0xf bank_mask:0xf bound_ctrl:1
	s_nop 1
	v_mov_b32_dpp v42, v41 row_mirror row_mask:0xf bank_mask:0xf bound_ctrl:1
	v_add_u32_e32 v42, v41, v42
	s_and_saveexec_b64 s[0:1], vcc
	ds_write_b32 v34, v42
	s_or_b64 exec, exec, s[0:1]
.Lu16_skip1:
	s_waitcnt lgkmcnt(0)
	v_readfirstlane_b32 s11, v4
	v_and_b32_e32 v48, 0x3fff, v4
	v_cndmask_b32_e64 v48, v48, v5, s[100:101]
	v_lshl_add_u32 v48, v48, 9, v43
	global_load_dwordx4 v[16:19], v48, s[70:71]
	v_cndmask_b32_e64 v48, v6, v7, s[100:101]
	v_lshl_add_u32 v48, v48, 9, v43
	global_load_dwordx4 v[20:23], v48, s[70:71]
	ds_read_b128 v[4:7], v136 offset:32
	s_waitcnt vmcnt(4)
	s_bfe_u32 s0, s12, 0x30010
	s_cmp_lg_u32 s0, 0
	s_cbranch_scc0 .Lu16_skip2
	s_bfe_u32 s1, s12, 0x2000e
	s_cmp_eq_u32 s1, s9
	s_cbranch_scc1 .Lu16_same2
	v_lshl_add_u32 v48, s1, 10, v52
	ds_read_b128 v[0:3], v48 offset:11072
	ds_read_b128 v[44:47], v48 offset:11088
	s_mov_b32 s9, s1
	s_waitcnt lgkmcnt(0)
.Lu16_same2:
	v_dot8_i32_i4 v39, v24, v0, 0
	v_dot8_i32_i4 v40, v28, v0, 0
	v_dot8_i32_i4 v35, v24, v2, 0
	v_dot8_i32_i4 v36, v28, v2, 0
	v_dot8_i32_i4 v39, v25, v1, v39
	v_dot8_i32_i4 v40, v29, v1, v40
	v_dot8_i32_i4 v35, v25, v3, v35
	v_dot8_i32_i4 v36, v29, v3, v36
	v_dot8_i32_i4 v39, v26, v44, v39
	v_dot8_i32_i4 v40, v30, v44, v40
	v_dot8_i32_i4 v35, v26, v46, v35
	v_dot8_i32_i4 v36, v30, v46, v36
	v_dot8_i32_i4 v39, v27, v45, v39
	v_dot8_i32_i4 v40, v31, v45, v40
	v_dot8_i32_i4 v35, v27, v47, v35
	v_dot8_i32_i4 v36, v31, v47, v36
	s_nop 2
	v_lshl_add_u32 v39, v39, 4, v35
	v_lshl_add_u32 v40, v40, 4, v36
	s_mulk_i32 s1, 0x690
	s_nop 0
	v_permlane16_swap_b32_e32 v39, v40
	v_add_u32_e32 v39, v39, v40
	s_lshr_b32 s4, s12, 17
	s_add_i32 s1, s90, s1
	v_add_u32_dpp v39, v39, v39 quad_perm:[1,0,3,2] row_mask:0xf bank_mask:0xf bound_ctrl:1
	s_and_b32 s4, s4, 0x7ffc
	s_add_i32 s1, s1, s4
	v_add_u32_dpp v39, v39, v39 quad_perm:[2,3,0,1] row_mask:0xf bank_mask:0xf bound_ctrl:1
	v_lshl_add_u32 v34, v33, 2, s1
	s_nop 0
	v_add_u32_dpp v41, v39, v39 row_half_mirror row_mask:0xf bank_mask:0xf bound_ctrl:1
	s_nop 1
	v_mov_b32_dpp v42, v41 row_mirror row_mask:0xf bank_mask:0xf bound_ctrl:1
	v_add_u32_e32 v42, v41, v42
	s_and_saveexec_b64 s[0:1], vcc
	ds_write_b32 v34, v42
	s_or_b64 exec, exec, s[0:1]
